# conversion item header: kernarg pointer loads waited once (was two serialized scalar-load round trips)
# speedup vs baseline: 1.0027x; 1.0002x over previous
.Lc3_have:
	s_cmpk_gt_i32 s19, 0x1fff
	v_lshrrev_b32_e32 v164, 4, v169
	v_and_b32_e32 v168, 15, v169
	v_lshrrev_b32_e32 v167, 3, v169
	s_cbranch_scc1 .Lc3_dn
	s_load_dwordx2 s[2:3], s[22:23], 0x60
	s_lshr_b32 s18, s19, 8
	s_lshl_b32 s21, s20, 5
	s_add_i32 s18, s18, s21
	s_bfe_u32 s21, s19, 0x30005
	s_and_b32 s26, s19, 31
	s_lshl_b32 s15, s18, 21
	s_waitcnt lgkmcnt(0)
	s_add_u32 s12, s24, s15
	s_addc_u32 s13, s25, 0
	s_lshl_b32 s15, s21, 7
	s_add_i32 s15, s15, 0x3b00000
	s_lshr_b32 s14, s26, 2
	s_lshl_b32 s14, s14, 18
	s_add_i32 s15, s15, s14
	s_and_b32 s14, s26, 3
	s_lshl_b32 s14, s14, 15
	s_add_i32 s15, s15, s14
	s_add_u32 s12, s12, s15
	s_addc_u32 s13, s13, 0
	s_lshl_b32 s18, s18, 23
	s_lshl_b32 s21, s21, 20
	s_add_i32 s18, s18, s21
	s_lshl_b32 s26, s26, 8
	s_add_i32 s18, s18, s26
	s_waitcnt lgkmcnt(0)
	s_add_u32 s2, s2, s18
	s_addc_u32 s3, s3, 0
	s_movk_i32 s14, 0x2000
	s_movk_i32 s15, 0x1000
	s_mov_b32 s16, 0x42000000
	v_lshlrev_b32_e32 v164, 18, v164
	v_and_b32_e32 v166, 1, v167
	v_lshlrev_b32_e32 v166, 17, v166
	v_lshrrev_b32_e32 v167, 1, v167
	v_lshl_or_b32 v167, v167, 10, v166
	s_branch .Lc3_go
.Lc3_dn:
	s_load_dwordx2 s[2:3], s[22:23], 0x70
	s_add_i32 s26, s19, 0xffffe000
	s_lshr_b32 s18, s26, 7
	s_lshl_b32 s21, s20, 5
	s_add_i32 s18, s18, s21
	s_bfe_u32 s21, s26, 0x30004
	s_and_b32 s26, s26, 15
	s_lshl_b32 s15, s18, 20
	s_waitcnt lgkmcnt(0)
	s_add_u32 s12, s24, s15
	s_addc_u32 s13, s25, 0
	s_lshl_b32 s15, s21, 7
	s_add_i32 s15, s15, 0x23b00000
	s_lshl_b32 s14, s26, 16
	s_add_i32 s15, s15, s14
	s_add_u32 s12, s12, s15
	s_addc_u32 s13, s13, 0
	s_lshl_b32 s18, s18, 22
	s_lshl_b32 s21, s21, 19
	s_add_i32 s18, s18, s21
	s_lshl_b32 s26, s26, 8
	s_add_i32 s18, s18, s26
	s_waitcnt lgkmcnt(0)
	s_add_u32 s2, s2, s18
	s_addc_u32 s3, s3, 0
	s_movk_i32 s14, 0x1000
	s_movk_i32 s15, 0x2000
	s_mov_b32 s16, 0x42800000
	v_lshlrev_b32_e32 v164, 17, v164
	v_lshlrev_b32_e32 v167, 10, v167
